# fp8 GEMM loops: last two LDS-DMA pieces of the 6-piece load segments issued from the following MFMA segment
# speedup vs baseline: 1.0165x; 1.0002x over previous
.LBB0_373:
	ds_read_b128 v[170:173], v1
	ds_read_b128 v[174:177], v156
	ds_read_b128 v[178:181], v157
	ds_read_b128 v[182:185], v158
	ds_read_b128 v[186:189], v159
	ds_read_b128 v[190:193], v160
	ds_read_b128 v[194:197], v161
	ds_read_b128 v[198:201], v162
	s_add_u32 s36, s6, 0xfffc0080
	s_addc_u32 s37, s7, -1
	s_cmp_eq_u32 s29, 12
	s_cselect_b32 s39, s31, s37
	s_cselect_b32 s38, s30, s36
	s_cselect_b32 s37, s35, s27
	s_cselect_b32 s36, s34, s9
	v_lshl_add_u64 v[148:149], s[6:7], 0, v[140:141]
	s_add_i32 m0, s43, 0xc000
	ds_read_b128 v[202:205], v163
	ds_read_b128 v[210:213], v163 offset:1024
	ds_read_b128 v[206:209], v164
	ds_read_b128 v[214:217], v164 offset:1024
	ds_read_b128 v[218:221], v163 offset:4096
	ds_read_b128 v[226:229], v163 offset:5120
	ds_read_b128 v[222:225], v164 offset:4096
	ds_read_b128 v[230:233], v164 offset:5120
	global_load_lds_dwordx4 v[148:149], off
	v_lshl_add_u64 v[148:149], s[6:7], 0, v[142:143]
	s_add_i32 m0, s43, 0xe000
	s_nop 0
	global_load_lds_dwordx4 v[148:149], off
	s_waitcnt vmcnt(8)
	s_waitcnt lgkmcnt(0)
	s_barrier
	s_setprio 1
	s_waitcnt lgkmcnt(0)
	v_mfma_scale_f32_32x32x64_f8f6f4 v[114:129], v[170:177], v[202:209], v[114:129], v165, v165 op_sel_hi:[0,0,0]
	v_mfma_scale_f32_32x32x64_f8f6f4 v[82:97], v[170:177], v[218:225], v[82:97], v165, v165 op_sel_hi:[0,0,0]
	v_mfma_scale_f32_32x32x64_f8f6f4 v[114:129], v[178:185], v[210:217], v[114:129], v165, v165 op_sel_hi:[0,0,0]
	v_mfma_scale_f32_32x32x64_f8f6f4 v[82:97], v[178:185], v[226:233], v[82:97], v165, v165 op_sel_hi:[0,0,0]
	s_setprio 0
	s_setprio 1
	v_mfma_scale_f32_32x32x64_f8f6f4 v[98:113], v[186:193], v[202:209], v[98:113], v165, v165 op_sel_hi:[0,0,0]
	v_mfma_scale_f32_32x32x64_f8f6f4 v[66:81], v[186:193], v[218:225], v[66:81], v165, v165 op_sel_hi:[0,0,0]
	v_mfma_scale_f32_32x32x64_f8f6f4 v[98:113], v[194:201], v[210:217], v[98:113], v165, v165 op_sel_hi:[0,0,0]
	v_mfma_scale_f32_32x32x64_f8f6f4 v[66:81], v[194:201], v[226:233], v[66:81], v165, v165 op_sel_hi:[0,0,0]
	s_setprio 0
	s_barrier
	s_add_i32 s55, s51, s42
	v_lshl_add_u64 v[148:149], s[36:37], 0, v[132:133]
	s_mov_b32 m0, s55
	ds_read_b128 v[202:205], v163 offset:16384
	ds_read_b128 v[210:213], v163 offset:17408
	ds_read_b128 v[206:209], v164 offset:16384
	ds_read_b128 v[214:217], v164 offset:17408
	ds_read_b128 v[218:221], v163 offset:20480
	ds_read_b128 v[226:229], v163 offset:21504
	ds_read_b128 v[222:225], v164 offset:20480
	ds_read_b128 v[230:233], v164 offset:21504
	global_load_lds_dwordx4 v[148:149], off
	s_add_i32 m0, s55, 0x2000
	s_add_u32 s56, s36, 0x40000
	v_lshl_add_u64 v[150:151], s[36:37], 0, v[136:137]
	s_addc_u32 s57, s37, 0
	s_add_i32 s55, s52, s42
	global_load_lds_dwordx4 v[150:151], off
	v_lshl_add_u64 v[152:153], s[56:57], 0, v[132:133]
	s_mov_b32 m0, s55
	v_lshl_add_u64 v[234:235], s[38:39], 0, v[134:135]
	global_load_lds_dwordx4 v[152:153], off
	v_lshl_add_u64 v[152:153], s[56:57], 0, v[136:137]
	s_add_i32 m0, s55, 0x2000
	s_nop 0
	global_load_lds_dwordx4 v[152:153], off
	s_waitcnt vmcnt(6)
	s_waitcnt lgkmcnt(0)
	s_barrier
	s_setprio 1
	s_waitcnt lgkmcnt(0)
	v_mfma_scale_f32_32x32x64_f8f6f4 v[50:65], v[170:177], v[202:209], v[50:65], v165, v165 op_sel_hi:[0,0,0]
	v_mfma_scale_f32_32x32x64_f8f6f4 v[18:33], v[170:177], v[218:225], v[18:33], v165, v165 op_sel_hi:[0,0,0]
	v_mfma_scale_f32_32x32x64_f8f6f4 v[50:65], v[178:185], v[210:217], v[50:65], v165, v165 op_sel_hi:[0,0,0]
	v_lshl_add_u64 v[152:153], s[38:39], 0, v[130:131]
	s_mov_b32 m0, s43
	s_nop 0
	global_load_lds_dwordx4 v[152:153], off
	v_mfma_scale_f32_32x32x64_f8f6f4 v[18:33], v[178:185], v[226:233], v[18:33], v165, v165 op_sel_hi:[0,0,0]
	s_setprio 0
	s_setprio 1
	v_mfma_scale_f32_32x32x64_f8f6f4 v[34:49], v[186:193], v[202:209], v[34:49], v165, v165 op_sel_hi:[0,0,0]
	v_mfma_scale_f32_32x32x64_f8f6f4 v[2:17], v[186:193], v[218:225], v[2:17], v165, v165 op_sel_hi:[0,0,0]
	s_mov_b32 m0, s44
	s_nop 0
	global_load_lds_dwordx4 v[234:235], off
	v_mfma_scale_f32_32x32x64_f8f6f4 v[34:49], v[194:201], v[210:217], v[34:49], v165, v165 op_sel_hi:[0,0,0]
	v_mfma_scale_f32_32x32x64_f8f6f4 v[2:17], v[194:201], v[226:233], v[2:17], v165, v165 op_sel_hi:[0,0,0]
	s_setprio 0
	s_barrier
	s_add_i32 s55, 0, 0x18000
	v_add_u32_e32 v138, s55, v154
	v_add_u32_e32 v174, s55, v155
	s_add_i32 s56, 0, 0x1c000
	ds_read_b128 v[170:173], v138
	ds_read_b128 v[174:177], v174
	ds_read_b128 v[178:181], v166
	ds_read_b128 v[182:185], v167
	v_add_u32_e32 v138, s56, v154
	v_add_u32_e32 v190, s56, v155
	ds_read_b128 v[186:189], v138
	ds_read_b128 v[190:193], v190
	ds_read_b128 v[194:197], v168
	ds_read_b128 v[198:201], v169
	s_add_u32 s38, s38, 0x40000
	s_addc_u32 s39, s39, 0
	s_mov_b32 m0, s45
	v_lshl_add_u64 v[236:237], s[38:39], 0, v[130:131]
	ds_read_b128 v[202:205], v163 offset:32768
	ds_read_b128 v[210:213], v163 offset:33792
	ds_read_b128 v[206:209], v164 offset:32768
	ds_read_b128 v[214:217], v164 offset:33792
	ds_read_b128 v[218:221], v163 offset:36864
	ds_read_b128 v[226:229], v163 offset:37888
	ds_read_b128 v[222:225], v164 offset:36864
	ds_read_b128 v[230:233], v164 offset:37888
	global_load_lds_dwordx4 v[236:237], off
	v_lshl_add_u64 v[236:237], s[38:39], 0, v[134:135]
	s_mov_b32 m0, s46
	s_nop 0
	global_load_lds_dwordx4 v[236:237], off
	s_waitcnt vmcnt(8)
	s_waitcnt lgkmcnt(0)
	s_barrier
	s_setprio 1
	s_waitcnt lgkmcnt(0)
	v_mfma_scale_f32_32x32x64_f8f6f4 v[114:129], v[170:177], v[202:209], v[114:129], v165, v165 op_sel_hi:[0,0,0]
	v_mfma_scale_f32_32x32x64_f8f6f4 v[82:97], v[170:177], v[218:225], v[82:97], v165, v165 op_sel_hi:[0,0,0]
	v_mfma_scale_f32_32x32x64_f8f6f4 v[114:129], v[178:185], v[210:217], v[114:129], v165, v165 op_sel_hi:[0,0,0]
	v_mfma_scale_f32_32x32x64_f8f6f4 v[82:97], v[178:185], v[226:233], v[82:97], v165, v165 op_sel_hi:[0,0,0]
	s_setprio 0
	s_setprio 1
	v_mfma_scale_f32_32x32x64_f8f6f4 v[98:113], v[186:193], v[202:209], v[98:113], v165, v165 op_sel_hi:[0,0,0]
	v_mfma_scale_f32_32x32x64_f8f6f4 v[66:81], v[186:193], v[218:225], v[66:81], v165, v165 op_sel_hi:[0,0,0]
	v_mfma_scale_f32_32x32x64_f8f6f4 v[98:113], v[194:201], v[210:217], v[98:113], v165, v165 op_sel_hi:[0,0,0]
	v_mfma_scale_f32_32x32x64_f8f6f4 v[66:81], v[194:201], v[226:233], v[66:81], v165, v165 op_sel_hi:[0,0,0]
	s_setprio 0
	s_barrier
	s_add_i32 s38, s55, s42
	v_lshl_add_u64 v[148:149], v[148:149], 0, s[16:17]
	s_mov_b32 m0, s38
	ds_read_b128 v[202:205], v163 offset:49152
	ds_read_b128 v[210:213], v163 offset:50176
	ds_read_b128 v[206:209], v164 offset:49152
	ds_read_b128 v[214:217], v164 offset:50176
	ds_read_b128 v[218:221], v163 offset:53248
	ds_read_b128 v[226:229], v163 offset:54272
	ds_read_b128 v[222:225], v164 offset:53248
	ds_read_b128 v[230:233], v164 offset:54272
	global_load_lds_dwordx4 v[148:149], off
	s_add_i32 m0, s38, 0x2000
	s_add_u32 s36, s36, 0x40080
	v_lshl_add_u64 v[148:149], v[150:151], 0, s[16:17]
	s_addc_u32 s37, s37, 0
	s_add_i32 s38, s56, s42
	global_load_lds_dwordx4 v[148:149], off
	v_lshl_add_u64 v[148:149], s[36:37], 0, v[132:133]
	s_mov_b32 m0, s38
	s_nop 0
	global_load_lds_dwordx4 v[148:149], off
	v_lshl_add_u64 v[148:149], s[36:37], 0, v[136:137]
	s_add_i32 m0, s38, 0x2000
	s_nop 0
	global_load_lds_dwordx4 v[148:149], off
	s_waitcnt vmcnt(6)
	s_waitcnt lgkmcnt(0)
	s_barrier
	s_setprio 1
	s_waitcnt lgkmcnt(0)
	v_mfma_scale_f32_32x32x64_f8f6f4 v[50:65], v[170:177], v[202:209], v[50:65], v165, v165 op_sel_hi:[0,0,0]
	v_mfma_scale_f32_32x32x64_f8f6f4 v[18:33], v[170:177], v[218:225], v[18:33], v165, v165 op_sel_hi:[0,0,0]
	v_mfma_scale_f32_32x32x64_f8f6f4 v[50:65], v[178:185], v[210:217], v[50:65], v165, v165 op_sel_hi:[0,0,0]
	v_lshl_add_u64 v[148:149], v[152:153], 0, s[16:17]
	s_mov_b32 m0, s47
	s_nop 0
	global_load_lds_dwordx4 v[148:149], off
	v_mfma_scale_f32_32x32x64_f8f6f4 v[18:33], v[178:185], v[226:233], v[18:33], v165, v165 op_sel_hi:[0,0,0]
	s_setprio 0
	s_setprio 1
	v_mfma_scale_f32_32x32x64_f8f6f4 v[34:49], v[186:193], v[202:209], v[34:49], v165, v165 op_sel_hi:[0,0,0]
	v_mfma_scale_f32_32x32x64_f8f6f4 v[2:17], v[186:193], v[218:225], v[2:17], v165, v165 op_sel_hi:[0,0,0]
	v_lshl_add_u64 v[148:149], v[234:235], 0, s[16:17]
	s_mov_b32 m0, s48
	s_nop 0
	global_load_lds_dwordx4 v[148:149], off
	v_mfma_scale_f32_32x32x64_f8f6f4 v[34:49], v[194:201], v[210:217], v[34:49], v165, v165 op_sel_hi:[0,0,0]
	v_mfma_scale_f32_32x32x64_f8f6f4 v[2:17], v[194:201], v[226:233], v[2:17], v165, v165 op_sel_hi:[0,0,0]
	s_setprio 0
	s_barrier
	s_add_i32 s29, s29, 2
	s_add_u32 s6, s6, 0x100
	s_addc_u32 s7, s7, 0
	s_add_u32 s9, s9, 0x100
	s_addc_u32 s27, s27, 0
	s_cmp_gt_u32 s29, 13
	s_cbranch_scc0 .LBB0_373
	s_and_b64 vcc, exec, s[18:19]
	s_cbranch_vccz .LBB0_376
	s_barrier

.LBB0_769:
	ds_read_b128 v[130:133], v159
	ds_read_b128 v[134:137], v160
	ds_read_b128 v[174:177], v161
	ds_read_b128 v[178:181], v162
	ds_read_b128 v[182:185], v163
	ds_read_b128 v[186:189], v164
	ds_read_b128 v[190:193], v165
	ds_read_b128 v[194:197], v166
	s_add_u32 s44, s42, 0xfffc0080
	s_addc_u32 s45, s43, -1
	s_cmp_eq_u32 s41, 12
	s_cselect_b32 s47, s37, s45
	s_cselect_b32 s46, s36, s44
	s_cselect_b32 s45, s39, s35
	s_cselect_b32 s44, s38, s31
	v_lshl_add_u64 v[154:155], s[42:43], 0, v[146:147]
	s_add_i32 m0, s51, 0xc000
	ds_read_b128 v[198:201], v167
	ds_read_b128 v[206:209], v167 offset:1024
	ds_read_b128 v[202:205], v168
	ds_read_b128 v[210:213], v168 offset:1024
	ds_read_b128 v[214:217], v167 offset:4096
	ds_read_b128 v[222:225], v167 offset:5120
	ds_read_b128 v[218:221], v168 offset:4096
	ds_read_b128 v[226:229], v168 offset:5120
	global_load_lds_dwordx4 v[154:155], off
	v_lshl_add_u64 v[154:155], s[42:43], 0, v[148:149]
	s_add_i32 m0, s51, 0xe000
	s_nop 0
	global_load_lds_dwordx4 v[154:155], off
	s_waitcnt vmcnt(8)
	s_waitcnt lgkmcnt(0)
	s_barrier
	s_setprio 1
	s_waitcnt lgkmcnt(0)
	v_mfma_scale_f32_32x32x64_f8f6f4 v[114:129], v[130:137], v[198:205], v[114:129], v169, v169 op_sel_hi:[0,0,0]
	v_mfma_scale_f32_32x32x64_f8f6f4 v[82:97], v[130:137], v[214:221], v[82:97], v169, v169 op_sel_hi:[0,0,0]
	v_mfma_scale_f32_32x32x64_f8f6f4 v[114:129], v[174:181], v[206:213], v[114:129], v169, v169 op_sel_hi:[0,0,0]
	v_mfma_scale_f32_32x32x64_f8f6f4 v[82:97], v[174:181], v[222:229], v[82:97], v169, v169 op_sel_hi:[0,0,0]
	s_setprio 0
	s_setprio 1
	v_mfma_scale_f32_32x32x64_f8f6f4 v[98:113], v[182:189], v[198:205], v[98:113], v169, v169 op_sel_hi:[0,0,0]
	v_mfma_scale_f32_32x32x64_f8f6f4 v[66:81], v[182:189], v[214:221], v[66:81], v169, v169 op_sel_hi:[0,0,0]
	v_mfma_scale_f32_32x32x64_f8f6f4 v[98:113], v[190:197], v[206:213], v[98:113], v169, v169 op_sel_hi:[0,0,0]
	v_mfma_scale_f32_32x32x64_f8f6f4 v[66:81], v[190:197], v[222:229], v[66:81], v169, v169 op_sel_hi:[0,0,0]
	s_setprio 0
	s_barrier
	s_add_i32 s65, s59, s50
	v_lshl_add_u64 v[154:155], s[44:45], 0, v[140:141]
	s_mov_b32 m0, s65
	ds_read_b128 v[198:201], v167 offset:16384
	ds_read_b128 v[206:209], v167 offset:17408
	ds_read_b128 v[202:205], v168 offset:16384
	ds_read_b128 v[210:213], v168 offset:17408
	ds_read_b128 v[214:217], v167 offset:20480
	ds_read_b128 v[222:225], v167 offset:21504
	ds_read_b128 v[218:221], v168 offset:20480
	ds_read_b128 v[226:229], v168 offset:21504
	global_load_lds_dwordx4 v[154:155], off
	s_add_i32 m0, s65, 0x2000
	s_add_u32 s66, s44, 0x40000
	v_lshl_add_u64 v[156:157], s[44:45], 0, v[144:145]
	s_addc_u32 s67, s45, 0
	s_add_i32 s65, s60, s50
	global_load_lds_dwordx4 v[156:157], off
	v_lshl_add_u64 v[230:231], s[66:67], 0, v[140:141]
	s_mov_b32 m0, s65
	v_lshl_add_u64 v[232:233], s[46:47], 0, v[142:143]
	global_load_lds_dwordx4 v[230:231], off
	v_lshl_add_u64 v[230:231], s[66:67], 0, v[144:145]
	s_add_i32 m0, s65, 0x2000
	s_nop 0
	global_load_lds_dwordx4 v[230:231], off
	s_waitcnt vmcnt(6)
	s_waitcnt lgkmcnt(0)
	s_barrier
	s_setprio 1
	s_waitcnt lgkmcnt(0)
	v_mfma_scale_f32_32x32x64_f8f6f4 v[50:65], v[130:137], v[198:205], v[50:65], v169, v169 op_sel_hi:[0,0,0]
	v_mfma_scale_f32_32x32x64_f8f6f4 v[18:33], v[130:137], v[214:221], v[18:33], v169, v169 op_sel_hi:[0,0,0]
	v_mfma_scale_f32_32x32x64_f8f6f4 v[50:65], v[174:181], v[206:213], v[50:65], v169, v169 op_sel_hi:[0,0,0]
	v_lshl_add_u64 v[230:231], s[46:47], 0, v[138:139]
	s_mov_b32 m0, s51
	s_nop 0
	global_load_lds_dwordx4 v[230:231], off
	v_mfma_scale_f32_32x32x64_f8f6f4 v[18:33], v[174:181], v[222:229], v[18:33], v169, v169 op_sel_hi:[0,0,0]
	s_setprio 0
	s_setprio 1
	v_mfma_scale_f32_32x32x64_f8f6f4 v[34:49], v[182:189], v[198:205], v[34:49], v169, v169 op_sel_hi:[0,0,0]
	v_mfma_scale_f32_32x32x64_f8f6f4 v[2:17], v[182:189], v[214:221], v[2:17], v169, v169 op_sel_hi:[0,0,0]
	s_mov_b32 m0, s52
	s_nop 0
	global_load_lds_dwordx4 v[232:233], off
	v_mfma_scale_f32_32x32x64_f8f6f4 v[34:49], v[190:197], v[206:213], v[34:49], v169, v169 op_sel_hi:[0,0,0]
	v_mfma_scale_f32_32x32x64_f8f6f4 v[2:17], v[190:197], v[222:229], v[2:17], v169, v169 op_sel_hi:[0,0,0]
	s_setprio 0
	s_barrier
	s_add_i32 s65, 0, 0x18000
	s_add_i32 s66, 0, 0x1c000
	v_add_u32_e32 v130, s65, v1
	v_add_u32_e32 v134, s65, v158
	v_add_u32_e32 v182, s66, v1
	v_add_u32_e32 v186, s66, v158
	ds_read_b128 v[130:133], v130
	ds_read_b128 v[134:137], v134
	ds_read_b128 v[174:177], v170
	ds_read_b128 v[178:181], v171
	ds_read_b128 v[182:185], v182
	ds_read_b128 v[186:189], v186
	ds_read_b128 v[190:193], v172
	ds_read_b128 v[194:197], v173
	s_add_u32 s46, s46, 0x40000
	s_addc_u32 s47, s47, 0
	s_mov_b32 m0, s53
	v_lshl_add_u64 v[234:235], s[46:47], 0, v[138:139]
	ds_read_b128 v[198:201], v167 offset:32768
	ds_read_b128 v[206:209], v167 offset:33792
	ds_read_b128 v[202:205], v168 offset:32768
	ds_read_b128 v[210:213], v168 offset:33792
	ds_read_b128 v[214:217], v167 offset:36864
	ds_read_b128 v[222:225], v167 offset:37888
	ds_read_b128 v[218:221], v168 offset:36864
	ds_read_b128 v[226:229], v168 offset:37888
	global_load_lds_dwordx4 v[234:235], off
	v_lshl_add_u64 v[234:235], s[46:47], 0, v[142:143]
	s_mov_b32 m0, s54
	s_nop 0
	global_load_lds_dwordx4 v[234:235], off
	s_waitcnt vmcnt(8)
	s_waitcnt lgkmcnt(0)
	s_barrier
	s_setprio 1
	s_waitcnt lgkmcnt(0)
	v_mfma_scale_f32_32x32x64_f8f6f4 v[114:129], v[130:137], v[198:205], v[114:129], v169, v169 op_sel_hi:[0,0,0]
	v_mfma_scale_f32_32x32x64_f8f6f4 v[82:97], v[130:137], v[214:221], v[82:97], v169, v169 op_sel_hi:[0,0,0]
	v_mfma_scale_f32_32x32x64_f8f6f4 v[114:129], v[174:181], v[206:213], v[114:129], v169, v169 op_sel_hi:[0,0,0]
	v_mfma_scale_f32_32x32x64_f8f6f4 v[82:97], v[174:181], v[222:229], v[82:97], v169, v169 op_sel_hi:[0,0,0]
	s_setprio 0
	s_setprio 1
	v_mfma_scale_f32_32x32x64_f8f6f4 v[98:113], v[182:189], v[198:205], v[98:113], v169, v169 op_sel_hi:[0,0,0]
	v_mfma_scale_f32_32x32x64_f8f6f4 v[66:81], v[182:189], v[214:221], v[66:81], v169, v169 op_sel_hi:[0,0,0]
	v_mfma_scale_f32_32x32x64_f8f6f4 v[98:113], v[190:197], v[206:213], v[98:113], v169, v169 op_sel_hi:[0,0,0]
	v_mfma_scale_f32_32x32x64_f8f6f4 v[66:81], v[190:197], v[222:229], v[66:81], v169, v169 op_sel_hi:[0,0,0]
	s_setprio 0
	s_barrier
	s_add_i32 s46, s65, s50
	v_lshl_add_u64 v[154:155], v[154:155], 0, s[14:15]
	s_mov_b32 m0, s46
	ds_read_b128 v[198:201], v167 offset:49152
	ds_read_b128 v[206:209], v167 offset:50176
	ds_read_b128 v[202:205], v168 offset:49152
	ds_read_b128 v[210:213], v168 offset:50176
	ds_read_b128 v[214:217], v167 offset:53248
	ds_read_b128 v[222:225], v167 offset:54272
	ds_read_b128 v[218:221], v168 offset:53248
	ds_read_b128 v[226:229], v168 offset:54272
	global_load_lds_dwordx4 v[154:155], off
	s_add_i32 m0, s46, 0x2000
	s_add_u32 s44, s44, 0x40080
	v_lshl_add_u64 v[154:155], v[156:157], 0, s[14:15]
	s_addc_u32 s45, s45, 0
	s_add_i32 s46, s66, s50
	global_load_lds_dwordx4 v[154:155], off
	v_lshl_add_u64 v[154:155], s[44:45], 0, v[140:141]
	s_mov_b32 m0, s46
	s_nop 0
	global_load_lds_dwordx4 v[154:155], off
	v_lshl_add_u64 v[154:155], s[44:45], 0, v[144:145]
	s_add_i32 m0, s46, 0x2000
	s_nop 0
	global_load_lds_dwordx4 v[154:155], off
	s_waitcnt vmcnt(6)
	s_waitcnt lgkmcnt(0)
	s_barrier
	s_setprio 1
	s_waitcnt lgkmcnt(0)
	v_mfma_scale_f32_32x32x64_f8f6f4 v[50:65], v[130:137], v[198:205], v[50:65], v169, v169 op_sel_hi:[0,0,0]
	v_mfma_scale_f32_32x32x64_f8f6f4 v[18:33], v[130:137], v[214:221], v[18:33], v169, v169 op_sel_hi:[0,0,0]
	v_mfma_scale_f32_32x32x64_f8f6f4 v[50:65], v[174:181], v[206:213], v[50:65], v169, v169 op_sel_hi:[0,0,0]
	v_lshl_add_u64 v[154:155], v[230:231], 0, s[14:15]
	s_mov_b32 m0, s56
	s_nop 0
	global_load_lds_dwordx4 v[154:155], off
	v_mfma_scale_f32_32x32x64_f8f6f4 v[18:33], v[174:181], v[222:229], v[18:33], v169, v169 op_sel_hi:[0,0,0]
	s_setprio 0
	s_setprio 1
	v_mfma_scale_f32_32x32x64_f8f6f4 v[34:49], v[182:189], v[198:205], v[34:49], v169, v169 op_sel_hi:[0,0,0]
	v_mfma_scale_f32_32x32x64_f8f6f4 v[2:17], v[182:189], v[214:221], v[2:17], v169, v169 op_sel_hi:[0,0,0]
	v_lshl_add_u64 v[154:155], v[232:233], 0, s[14:15]
	s_mov_b32 m0, s57
	s_nop 0
	global_load_lds_dwordx4 v[154:155], off
	v_mfma_scale_f32_32x32x64_f8f6f4 v[34:49], v[190:197], v[206:213], v[34:49], v169, v169 op_sel_hi:[0,0,0]
	v_mfma_scale_f32_32x32x64_f8f6f4 v[2:17], v[190:197], v[222:229], v[2:17], v169, v169 op_sel_hi:[0,0,0]
	s_setprio 0
	s_barrier
	s_add_i32 s41, s41, 2
	s_add_u32 s42, s42, 0x100
	s_addc_u32 s43, s43, 0
	s_add_u32 s31, s31, 0x100
	s_addc_u32 s35, s35, 0
	s_cmp_gt_u32 s41, 13
	s_cbranch_scc0 .LBB0_769
	s_and_b64 vcc, exec, s[16:17]
	s_cbranch_vccz .LBB0_772
	s_barrier

.LBB0_925:
	s_waitcnt vmcnt(8)
	s_add_u32 s36, s30, 0x80
	s_waitcnt lgkmcnt(0)
	s_addc_u32 s37, s31, 0
	s_and_b64 s[34:35], s[34:35], exec
	v_mov_b32_e32 v205, v199
	s_cselect_b32 s37, s11, s37
	s_cselect_b32 s36, s10, s36
	s_cselect_b32 s35, s23, s27
	s_cselect_b32 s34, s22, s25
	s_barrier
	s_setprio 1
	s_waitcnt lgkmcnt(0)
	v_mfma_scale_f32_32x32x64_f8f6f4 v[114:129], v[154:161], v[178:185], v[114:129], v224, v224 op_sel_hi:[0,0,0]
	v_mfma_scale_f32_32x32x64_f8f6f4 v[82:97], v[154:161], v[186:193], v[82:97], v224, v224 op_sel_hi:[0,0,0]
	v_mfma_scale_f32_32x32x64_f8f6f4 v[114:129], v[146:153], v[162:169], v[114:129], v224, v224 op_sel_hi:[0,0,0]
	v_mfma_scale_f32_32x32x64_f8f6f4 v[82:97], v[146:153], v[170:177], v[82:97], v224, v224 op_sel_hi:[0,0,0]
	s_setprio 0
	s_setprio 1
	v_mfma_scale_f32_32x32x64_f8f6f4 v[98:113], v[138:145], v[178:185], v[98:113], v224, v224 op_sel_hi:[0,0,0]
	v_mfma_scale_f32_32x32x64_f8f6f4 v[66:81], v[138:145], v[186:193], v[66:81], v224, v224 op_sel_hi:[0,0,0]
	v_mfma_scale_f32_32x32x64_f8f6f4 v[98:113], v[130:137], v[162:169], v[98:113], v224, v224 op_sel_hi:[0,0,0]
	v_mfma_scale_f32_32x32x64_f8f6f4 v[66:81], v[130:137], v[170:177], v[66:81], v224, v224 op_sel_hi:[0,0,0]
	s_setprio 0
	s_barrier
	s_mov_b32 m0, s42
	v_lshl_add_u64 v[232:233], s[34:35], 0, v[194:195]
	s_add_u32 s66, s34, 0x40000
	ds_read_b128 v[162:165], v221 offset:16384
	ds_read_b128 v[170:173], v221 offset:17408
	ds_read_b128 v[166:169], v223 offset:16384
	ds_read_b128 v[174:177], v223 offset:17408
	ds_read_b128 v[178:181], v221 offset:20480
	ds_read_b128 v[186:189], v221 offset:21504
	ds_read_b128 v[182:185], v223 offset:20480
	ds_read_b128 v[190:193], v223 offset:21504
	global_load_lds_dwordx4 v[232:233], off
	v_lshl_add_u64 v[234:235], s[34:35], 0, v[196:197]
	s_mov_b32 m0, s43
	s_addc_u32 s67, s35, 0
	global_load_lds_dwordx4 v[234:235], off
	v_lshl_add_u64 v[236:237], s[66:67], 0, v[194:195]
	s_mov_b32 m0, s44
	v_mov_b32_e32 v203, v199
	global_load_lds_dwordx4 v[236:237], off
	v_lshl_add_u64 v[236:237], s[66:67], 0, v[196:197]
	s_mov_b32 m0, s45
	v_lshl_add_u64 v[238:239], s[36:37], 0, v[202:203]
	global_load_lds_dwordx4 v[236:237], off
	s_waitcnt vmcnt(6)
	s_waitcnt lgkmcnt(0)
	s_barrier
	s_setprio 1
	s_waitcnt lgkmcnt(0)
	v_mfma_scale_f32_32x32x64_f8f6f4 v[50:65], v[154:161], v[162:169], v[50:65], v224, v224 op_sel_hi:[0,0,0]
	v_mfma_scale_f32_32x32x64_f8f6f4 v[18:33], v[154:161], v[178:185], v[18:33], v224, v224 op_sel_hi:[0,0,0]
	v_mfma_scale_f32_32x32x64_f8f6f4 v[50:65], v[146:153], v[170:177], v[50:65], v224, v224 op_sel_hi:[0,0,0]
	s_mov_b32 m0, s41
	v_lshl_add_u64 v[236:237], s[36:37], 0, v[198:199]
	global_load_lds_dwordx4 v198, s[36:37]
	v_mfma_scale_f32_32x32x64_f8f6f4 v[18:33], v[146:153], v[186:193], v[18:33], v224, v224 op_sel_hi:[0,0,0]
	s_setprio 0
	s_setprio 1
	v_mfma_scale_f32_32x32x64_f8f6f4 v[34:49], v[138:145], v[162:169], v[34:49], v224, v224 op_sel_hi:[0,0,0]
	v_mfma_scale_f32_32x32x64_f8f6f4 v[2:17], v[138:145], v[178:185], v[2:17], v224, v224 op_sel_hi:[0,0,0]
	s_mov_b32 m0, s46
	s_nop 0
	global_load_lds_dwordx4 v202, s[36:37]
	v_mfma_scale_f32_32x32x64_f8f6f4 v[34:49], v[130:137], v[170:177], v[34:49], v224, v224 op_sel_hi:[0,0,0]
	v_mfma_scale_f32_32x32x64_f8f6f4 v[2:17], v[130:137], v[186:193], v[2:17], v224, v224 op_sel_hi:[0,0,0]
	s_setprio 0
	s_barrier
	s_add_i32 s65, 0, 0x18000
	s_add_i32 s66, 0, 0x1c000
	v_add_u32_e32 v130, s65, v210
	v_add_u32_e32 v134, s65, v211
	v_add_u32_e32 v138, s57, v210
	v_add_u32_e32 v142, s57, v211
	v_add_u32_e32 v146, s66, v210
	v_add_u32_e32 v150, s66, v211
	v_add_u32_e32 v154, s58, v210
	v_add_u32_e32 v158, s58, v211
	ds_read_b128 v[130:133], v130
	ds_read_b128 v[134:137], v134
	ds_read_b128 v[138:141], v138
	ds_read_b128 v[142:145], v142
	ds_read_b128 v[146:149], v146
	ds_read_b128 v[150:153], v150
	ds_read_b128 v[154:157], v154
	ds_read_b128 v[158:161], v158
	s_mov_b32 m0, s47
	v_lshl_add_u64 v[240:241], s[36:37], 0, v[200:201]
	ds_read_b128 v[162:165], v221 offset:32768
	ds_read_b128 v[170:173], v221 offset:33792
	ds_read_b128 v[166:169], v223 offset:32768
	ds_read_b128 v[174:177], v223 offset:33792
	ds_read_b128 v[178:181], v221 offset:36864
	ds_read_b128 v[186:189], v221 offset:37888
	ds_read_b128 v[182:185], v223 offset:36864
	ds_read_b128 v[190:193], v223 offset:37888
	global_load_lds_dwordx4 v[240:241], off
	v_lshl_add_u64 v[240:241], s[36:37], 0, v[204:205]
	s_mov_b32 m0, s48
	s_nop 0
	global_load_lds_dwordx4 v[240:241], off
	s_waitcnt vmcnt(8)
	s_waitcnt lgkmcnt(0)
	s_barrier
	s_setprio 1
	s_waitcnt lgkmcnt(0)
	v_mfma_scale_f32_32x32x64_f8f6f4 v[114:129], v[130:137], v[162:169], v[114:129], v224, v224 op_sel_hi:[0,0,0]
	v_mfma_scale_f32_32x32x64_f8f6f4 v[82:97], v[130:137], v[178:185], v[82:97], v224, v224 op_sel_hi:[0,0,0]
	v_mfma_scale_f32_32x32x64_f8f6f4 v[114:129], v[138:145], v[170:177], v[114:129], v224, v224 op_sel_hi:[0,0,0]
	v_mfma_scale_f32_32x32x64_f8f6f4 v[82:97], v[138:145], v[186:193], v[82:97], v224, v224 op_sel_hi:[0,0,0]
	s_setprio 0
	s_setprio 1
	v_mfma_scale_f32_32x32x64_f8f6f4 v[98:113], v[146:153], v[162:169], v[98:113], v224, v224 op_sel_hi:[0,0,0]
	v_mfma_scale_f32_32x32x64_f8f6f4 v[66:81], v[146:153], v[178:185], v[66:81], v224, v224 op_sel_hi:[0,0,0]
	v_mfma_scale_f32_32x32x64_f8f6f4 v[98:113], v[154:161], v[170:177], v[98:113], v224, v224 op_sel_hi:[0,0,0]
	v_mfma_scale_f32_32x32x64_f8f6f4 v[66:81], v[154:161], v[186:193], v[66:81], v224, v224 op_sel_hi:[0,0,0]
	s_setprio 0
	s_barrier
	s_add_i32 s36, s65, s40
	v_lshl_add_u64 v[232:233], v[232:233], 0, s[14:15]
	s_mov_b32 m0, s36
	ds_read_b128 v[162:165], v221 offset:49152
	ds_read_b128 v[170:173], v221 offset:50176
	ds_read_b128 v[166:169], v223 offset:49152
	ds_read_b128 v[174:177], v223 offset:50176
	ds_read_b128 v[178:181], v221 offset:53248
	ds_read_b128 v[186:189], v221 offset:54272
	ds_read_b128 v[182:185], v223 offset:53248
	ds_read_b128 v[190:193], v223 offset:54272
	global_load_lds_dwordx4 v[232:233], off
	s_add_i32 m0, s36, 0x2000
	s_add_u32 s34, s34, 0x40080
	v_lshl_add_u64 v[232:233], v[234:235], 0, s[14:15]
	s_addc_u32 s35, s35, 0
	s_add_i32 s36, s66, s40
	global_load_lds_dwordx4 v[232:233], off
	v_lshl_add_u64 v[232:233], s[34:35], 0, v[194:195]
	s_mov_b32 m0, s36
	s_nop 0
	global_load_lds_dwordx4 v[232:233], off
	v_lshl_add_u64 v[232:233], s[34:35], 0, v[196:197]
	s_add_i32 m0, s36, 0x2000
	s_nop 0
	global_load_lds_dwordx4 v[232:233], off
	s_waitcnt vmcnt(6)
	s_waitcnt lgkmcnt(0)
	s_barrier
	s_setprio 1
	s_waitcnt lgkmcnt(0)
	v_mfma_scale_f32_32x32x64_f8f6f4 v[50:65], v[130:137], v[162:169], v[50:65], v224, v224 op_sel_hi:[0,0,0]
	v_mfma_scale_f32_32x32x64_f8f6f4 v[18:33], v[130:137], v[178:185], v[18:33], v224, v224 op_sel_hi:[0,0,0]
	v_mfma_scale_f32_32x32x64_f8f6f4 v[50:65], v[138:145], v[170:177], v[50:65], v224, v224 op_sel_hi:[0,0,0]
	v_lshl_add_u64 v[232:233], v[236:237], 0, s[14:15]
	s_mov_b32 m0, s52
	s_nop 0
	global_load_lds_dwordx4 v[232:233], off
	v_mfma_scale_f32_32x32x64_f8f6f4 v[18:33], v[138:145], v[186:193], v[18:33], v224, v224 op_sel_hi:[0,0,0]
	s_setprio 0
	s_setprio 1
	v_mfma_scale_f32_32x32x64_f8f6f4 v[34:49], v[146:153], v[162:169], v[34:49], v224, v224 op_sel_hi:[0,0,0]
	v_mfma_scale_f32_32x32x64_f8f6f4 v[2:17], v[146:153], v[178:185], v[2:17], v224, v224 op_sel_hi:[0,0,0]
	v_lshl_add_u64 v[232:233], v[238:239], 0, s[14:15]
	s_mov_b32 m0, s53
	s_nop 0
	global_load_lds_dwordx4 v[232:233], off
	v_mfma_scale_f32_32x32x64_f8f6f4 v[34:49], v[154:161], v[170:177], v[34:49], v224, v224 op_sel_hi:[0,0,0]
	v_mfma_scale_f32_32x32x64_f8f6f4 v[2:17], v[154:161], v[186:193], v[2:17], v224, v224 op_sel_hi:[0,0,0]
	s_setprio 0
	s_barrier
	s_add_i32 s64, s64, 2
	s_add_u32 s30, s30, 0x100
	s_addc_u32 s31, s31, 0
	s_add_u32 s25, s25, 0x100
	s_addc_u32 s27, s27, 0
	s_cmp_gt_u32 s64, 13
	s_cbranch_scc1 .LBB0_928

.LBB0_1014:
	ds_read_b128 v[168:171], v150
	ds_read_b128 v[172:175], v151
	ds_read_b128 v[176:179], v152
	ds_read_b128 v[180:183], v153
	ds_read_b128 v[184:187], v154
	ds_read_b128 v[188:191], v155
	ds_read_b128 v[192:195], v156
	ds_read_b128 v[196:199], v157
	s_add_u32 s30, s28, 0xfffe0080
	s_addc_u32 s31, s29, -1
	s_cmp_eq_u32 s58, 4
	s_cselect_b32 s35, s21, s31
	s_cselect_b32 s34, s20, s30
	s_cselect_b32 s31, s23, s27
	s_cselect_b32 s30, s22, s25
	v_lshl_add_u64 v[144:145], s[28:29], 0, v[140:141]
	s_add_i32 m0, s37, 0xc000
	ds_read_b128 v[200:203], v158
	ds_read_b128 v[208:211], v158 offset:1024
	ds_read_b128 v[204:207], v159
	ds_read_b128 v[212:215], v159 offset:1024
	ds_read_b128 v[216:219], v158 offset:4096
	ds_read_b128 v[224:227], v158 offset:5120
	ds_read_b128 v[220:223], v159 offset:4096
	ds_read_b128 v[228:231], v159 offset:5120
	global_load_lds_dwordx4 v[144:145], off
	v_lshl_add_u64 v[144:145], s[28:29], 0, v[142:143]
	s_add_i32 m0, s37, 0xe000
	s_nop 0
	global_load_lds_dwordx4 v[144:145], off
	s_waitcnt vmcnt(8)
	s_waitcnt lgkmcnt(0)
	s_barrier
	s_setprio 1
	s_waitcnt lgkmcnt(0)
	v_mfma_scale_f32_32x32x64_f8f6f4 v[114:129], v[168:175], v[200:207], v[114:129], v160, v160 op_sel_hi:[0,0,0]
	v_mfma_scale_f32_32x32x64_f8f6f4 v[82:97], v[168:175], v[216:223], v[82:97], v160, v160 op_sel_hi:[0,0,0]
	v_mfma_scale_f32_32x32x64_f8f6f4 v[114:129], v[176:183], v[208:215], v[114:129], v160, v160 op_sel_hi:[0,0,0]
	v_mfma_scale_f32_32x32x64_f8f6f4 v[82:97], v[176:183], v[224:231], v[82:97], v160, v160 op_sel_hi:[0,0,0]
	s_setprio 0
	s_setprio 1
	v_mfma_scale_f32_32x32x64_f8f6f4 v[98:113], v[184:191], v[200:207], v[98:113], v160, v160 op_sel_hi:[0,0,0]
	v_mfma_scale_f32_32x32x64_f8f6f4 v[66:81], v[184:191], v[216:223], v[66:81], v160, v160 op_sel_hi:[0,0,0]
	v_mfma_scale_f32_32x32x64_f8f6f4 v[98:113], v[192:199], v[208:215], v[98:113], v160, v160 op_sel_hi:[0,0,0]
	v_mfma_scale_f32_32x32x64_f8f6f4 v[66:81], v[192:199], v[224:231], v[66:81], v160, v160 op_sel_hi:[0,0,0]
	s_setprio 0
	s_barrier
	s_add_i32 s59, s51, s36
	v_lshl_add_u64 v[144:145], s[30:31], 0, v[132:133]
	s_mov_b32 m0, s59
	ds_read_b128 v[200:203], v158 offset:16384
	ds_read_b128 v[208:211], v158 offset:17408
	ds_read_b128 v[204:207], v159 offset:16384
	ds_read_b128 v[212:215], v159 offset:17408
	ds_read_b128 v[216:219], v158 offset:20480
	ds_read_b128 v[224:227], v158 offset:21504
	ds_read_b128 v[220:223], v159 offset:20480
	ds_read_b128 v[228:231], v159 offset:21504
	global_load_lds_dwordx4 v[144:145], off
	s_add_i32 m0, s59, 0x2000
	s_add_u32 s60, s30, 0x20000
	v_lshl_add_u64 v[146:147], s[30:31], 0, v[136:137]
	s_addc_u32 s61, s31, 0
	s_add_i32 s59, s52, s36
	global_load_lds_dwordx4 v[146:147], off
	v_lshl_add_u64 v[232:233], s[60:61], 0, v[132:133]
	s_mov_b32 m0, s59
	v_lshl_add_u64 v[234:235], s[34:35], 0, v[134:135]
	global_load_lds_dwordx4 v[232:233], off
	v_lshl_add_u64 v[232:233], s[60:61], 0, v[136:137]
	s_add_i32 m0, s59, 0x2000
	s_nop 0
	global_load_lds_dwordx4 v[232:233], off
	s_waitcnt vmcnt(6)
	s_waitcnt lgkmcnt(0)
	s_barrier
	s_setprio 1
	s_waitcnt lgkmcnt(0)
	v_mfma_scale_f32_32x32x64_f8f6f4 v[50:65], v[168:175], v[200:207], v[50:65], v160, v160 op_sel_hi:[0,0,0]
	v_mfma_scale_f32_32x32x64_f8f6f4 v[18:33], v[168:175], v[216:223], v[18:33], v160, v160 op_sel_hi:[0,0,0]
	v_mfma_scale_f32_32x32x64_f8f6f4 v[50:65], v[176:183], v[208:215], v[50:65], v160, v160 op_sel_hi:[0,0,0]
	v_lshl_add_u64 v[232:233], s[34:35], 0, v[130:131]
	s_mov_b32 m0, s37
	s_nop 0
	global_load_lds_dwordx4 v[232:233], off
	v_mfma_scale_f32_32x32x64_f8f6f4 v[18:33], v[176:183], v[224:231], v[18:33], v160, v160 op_sel_hi:[0,0,0]
	s_setprio 0
	s_setprio 1
	v_mfma_scale_f32_32x32x64_f8f6f4 v[34:49], v[184:191], v[200:207], v[34:49], v160, v160 op_sel_hi:[0,0,0]
	v_mfma_scale_f32_32x32x64_f8f6f4 v[2:17], v[184:191], v[216:223], v[2:17], v160, v160 op_sel_hi:[0,0,0]
	s_mov_b32 m0, s38
	s_nop 0
	global_load_lds_dwordx4 v[234:235], off
	v_mfma_scale_f32_32x32x64_f8f6f4 v[34:49], v[192:199], v[208:215], v[34:49], v160, v160 op_sel_hi:[0,0,0]
	v_mfma_scale_f32_32x32x64_f8f6f4 v[2:17], v[192:199], v[224:231], v[2:17], v160, v160 op_sel_hi:[0,0,0]
	s_setprio 0
	s_barrier
	s_add_i32 s59, 0, 0x18000
	v_add_u32_e32 v167, s59, v1
	v_add_u32_e32 v172, s59, v148
	s_add_i32 s60, 0, 0x1c000
	ds_read_b128 v[168:171], v167
	ds_read_b128 v[172:175], v172
	ds_read_b128 v[176:179], v161
	ds_read_b128 v[180:183], v162
	v_add_u32_e32 v167, s60, v1
	v_add_u32_e32 v188, s60, v148
	ds_read_b128 v[184:187], v167
	ds_read_b128 v[188:191], v188
	ds_read_b128 v[192:195], v163
	ds_read_b128 v[196:199], v164
	s_add_u32 s34, s34, 0x20000
	s_addc_u32 s35, s35, 0
	s_mov_b32 m0, s39
	v_lshl_add_u64 v[236:237], s[34:35], 0, v[130:131]
	ds_read_b128 v[200:203], v158 offset:32768
	ds_read_b128 v[208:211], v158 offset:33792
	ds_read_b128 v[204:207], v159 offset:32768
	ds_read_b128 v[212:215], v159 offset:33792
	ds_read_b128 v[216:219], v158 offset:36864
	ds_read_b128 v[224:227], v158 offset:37888
	ds_read_b128 v[220:223], v159 offset:36864
	ds_read_b128 v[228:231], v159 offset:37888
	global_load_lds_dwordx4 v[236:237], off
	v_lshl_add_u64 v[236:237], s[34:35], 0, v[134:135]
	s_mov_b32 m0, s40
	s_nop 0
	global_load_lds_dwordx4 v[236:237], off
	s_waitcnt vmcnt(8)
	s_waitcnt lgkmcnt(0)
	s_barrier
	s_setprio 1
	s_waitcnt lgkmcnt(0)
	v_mfma_scale_f32_32x32x64_f8f6f4 v[114:129], v[168:175], v[200:207], v[114:129], v160, v160 op_sel_hi:[0,0,0]
	v_mfma_scale_f32_32x32x64_f8f6f4 v[82:97], v[168:175], v[216:223], v[82:97], v160, v160 op_sel_hi:[0,0,0]
	v_mfma_scale_f32_32x32x64_f8f6f4 v[114:129], v[176:183], v[208:215], v[114:129], v160, v160 op_sel_hi:[0,0,0]
	v_mfma_scale_f32_32x32x64_f8f6f4 v[82:97], v[176:183], v[224:231], v[82:97], v160, v160 op_sel_hi:[0,0,0]
	s_setprio 0
	s_setprio 1
	v_mfma_scale_f32_32x32x64_f8f6f4 v[98:113], v[184:191], v[200:207], v[98:113], v160, v160 op_sel_hi:[0,0,0]
	v_mfma_scale_f32_32x32x64_f8f6f4 v[66:81], v[184:191], v[216:223], v[66:81], v160, v160 op_sel_hi:[0,0,0]
	v_mfma_scale_f32_32x32x64_f8f6f4 v[98:113], v[192:199], v[208:215], v[98:113], v160, v160 op_sel_hi:[0,0,0]
	v_mfma_scale_f32_32x32x64_f8f6f4 v[66:81], v[192:199], v[224:231], v[66:81], v160, v160 op_sel_hi:[0,0,0]
	s_setprio 0
	s_barrier
	s_add_i32 s34, s59, s36
	v_lshl_add_u64 v[144:145], v[144:145], 0, s[12:13]
	s_mov_b32 m0, s34
	ds_read_b128 v[200:203], v158 offset:49152
	ds_read_b128 v[208:211], v158 offset:50176
	ds_read_b128 v[204:207], v159 offset:49152
	ds_read_b128 v[212:215], v159 offset:50176
	ds_read_b128 v[216:219], v158 offset:53248
	ds_read_b128 v[224:227], v158 offset:54272
	ds_read_b128 v[220:223], v159 offset:53248
	ds_read_b128 v[228:231], v159 offset:54272
	global_load_lds_dwordx4 v[144:145], off
	s_add_i32 m0, s34, 0x2000
	s_add_u32 s30, s30, 0x20080
	v_lshl_add_u64 v[144:145], v[146:147], 0, s[12:13]
	s_addc_u32 s31, s31, 0
	s_add_i32 s34, s60, s36
	global_load_lds_dwordx4 v[144:145], off
	v_lshl_add_u64 v[144:145], s[30:31], 0, v[132:133]
	s_mov_b32 m0, s34
	s_nop 0
	global_load_lds_dwordx4 v[144:145], off
	v_lshl_add_u64 v[144:145], s[30:31], 0, v[136:137]
	s_add_i32 m0, s34, 0x2000
	s_nop 0
	global_load_lds_dwordx4 v[144:145], off
	s_waitcnt vmcnt(6)
	s_waitcnt lgkmcnt(0)
	s_barrier
	s_setprio 1
	s_waitcnt lgkmcnt(0)
	v_mfma_scale_f32_32x32x64_f8f6f4 v[50:65], v[168:175], v[200:207], v[50:65], v160, v160 op_sel_hi:[0,0,0]
	v_mfma_scale_f32_32x32x64_f8f6f4 v[18:33], v[168:175], v[216:223], v[18:33], v160, v160 op_sel_hi:[0,0,0]
	v_mfma_scale_f32_32x32x64_f8f6f4 v[50:65], v[176:183], v[208:215], v[50:65], v160, v160 op_sel_hi:[0,0,0]
	v_lshl_add_u64 v[144:145], v[232:233], 0, s[12:13]
	s_mov_b32 m0, s46
	s_nop 0
	global_load_lds_dwordx4 v[144:145], off
	v_mfma_scale_f32_32x32x64_f8f6f4 v[18:33], v[176:183], v[224:231], v[18:33], v160, v160 op_sel_hi:[0,0,0]
	s_setprio 0
	s_setprio 1
	v_mfma_scale_f32_32x32x64_f8f6f4 v[34:49], v[184:191], v[200:207], v[34:49], v160, v160 op_sel_hi:[0,0,0]
	v_mfma_scale_f32_32x32x64_f8f6f4 v[2:17], v[184:191], v[216:223], v[2:17], v160, v160 op_sel_hi:[0,0,0]
	v_lshl_add_u64 v[144:145], v[234:235], 0, s[12:13]
	s_mov_b32 m0, s47
	s_nop 0
	global_load_lds_dwordx4 v[144:145], off
	v_mfma_scale_f32_32x32x64_f8f6f4 v[34:49], v[192:199], v[208:215], v[34:49], v160, v160 op_sel_hi:[0,0,0]
	v_mfma_scale_f32_32x32x64_f8f6f4 v[2:17], v[192:199], v[224:231], v[2:17], v160, v160 op_sel_hi:[0,0,0]
	s_setprio 0
	s_barrier
	s_add_i32 s58, s58, 2
	s_add_u32 s28, s28, 0x100
	s_addc_u32 s29, s29, 0
	s_add_u32 s25, s25, 0x100
	s_addc_u32 s27, s27, 0
	s_cmp_gt_u32 s58, 5
	s_cbranch_scc0 .LBB0_1014
	s_and_b64 vcc, exec, s[14:15]
	s_cbranch_vccz .LBB0_1017
	s_barrier

.LBB0_1147:
	v_add_u32_e32 v130, s63, v1
	v_add_u32_e32 v134, s63, v177
	v_add_u32_e32 v146, s64, v1
	v_add_u32_e32 v150, s64, v177
	ds_read_b128 v[130:133], v130
	ds_read_b128 v[134:137], v134
	ds_read_b128 v[138:141], v179
	ds_read_b128 v[142:145], v181
	ds_read_b128 v[146:149], v146
	ds_read_b128 v[150:153], v150
	ds_read_b128 v[154:157], v183
	ds_read_b128 v[158:161], v190
	s_add_u32 s42, s40, 0xfffc0080
	s_addc_u32 s43, s41, -1
	s_cmp_eq_u32 s35, 12
	s_cselect_b32 s45, s37, s43
	s_cselect_b32 s44, s36, s42
	s_cselect_b32 s43, s39, s31
	s_cselect_b32 s42, s38, s7
	v_lshl_add_u64 v[184:185], s[40:41], 0, v[172:173]
	s_add_i32 m0, s51, 0xc000
	ds_read_b128 v[208:211], v191
	ds_read_b128 v[216:219], v191 offset:1024
	ds_read_b128 v[212:215], v192
	ds_read_b128 v[220:223], v192 offset:1024
	ds_read_b128 v[224:227], v191 offset:4096
	ds_read_b128 v[232:235], v191 offset:5120
	ds_read_b128 v[228:231], v192 offset:4096
	ds_read_b128 v[236:239], v192 offset:5120
	global_load_lds_dwordx4 v[184:185], off
	v_lshl_add_u64 v[184:185], s[40:41], 0, v[174:175]
	s_add_i32 m0, s51, 0xe000
	s_nop 0
	global_load_lds_dwordx4 v[184:185], off
	s_waitcnt vmcnt(8)
	s_waitcnt lgkmcnt(0)
	s_barrier
	s_setprio 1
	s_waitcnt lgkmcnt(0)
	v_mfma_scale_f32_32x32x64_f8f6f4 v[114:129], v[130:137], v[208:215], v[114:129], v193, v193 op_sel_hi:[0,0,0]
	v_mfma_scale_f32_32x32x64_f8f6f4 v[82:97], v[130:137], v[224:231], v[82:97], v193, v193 op_sel_hi:[0,0,0]
	v_mfma_scale_f32_32x32x64_f8f6f4 v[114:129], v[138:145], v[216:223], v[114:129], v193, v193 op_sel_hi:[0,0,0]
	v_mfma_scale_f32_32x32x64_f8f6f4 v[82:97], v[138:145], v[232:239], v[82:97], v193, v193 op_sel_hi:[0,0,0]
	s_setprio 0
	s_setprio 1
	v_mfma_scale_f32_32x32x64_f8f6f4 v[98:113], v[146:153], v[208:215], v[98:113], v193, v193 op_sel_hi:[0,0,0]
	v_mfma_scale_f32_32x32x64_f8f6f4 v[66:81], v[146:153], v[224:231], v[66:81], v193, v193 op_sel_hi:[0,0,0]
	v_mfma_scale_f32_32x32x64_f8f6f4 v[98:113], v[154:161], v[216:223], v[98:113], v193, v193 op_sel_hi:[0,0,0]
	v_mfma_scale_f32_32x32x64_f8f6f4 v[66:81], v[154:161], v[232:239], v[66:81], v193, v193 op_sel_hi:[0,0,0]
	s_setprio 0
	s_barrier
	s_add_i32 s46, s63, s50
	v_lshl_add_u64 v[184:185], s[42:43], 0, v[164:165]
	s_mov_b32 m0, s46
	ds_read_b128 v[208:211], v191 offset:16384
	ds_read_b128 v[216:219], v191 offset:17408
	ds_read_b128 v[212:215], v192 offset:16384
	ds_read_b128 v[220:223], v192 offset:17408
	ds_read_b128 v[224:227], v191 offset:20480
	ds_read_b128 v[232:235], v191 offset:21504
	ds_read_b128 v[228:231], v192 offset:20480
	ds_read_b128 v[236:239], v192 offset:21504
	global_load_lds_dwordx4 v[184:185], off
	s_add_i32 m0, s46, 0x2000
	s_add_u32 s46, s42, 0x40000
	v_lshl_add_u64 v[186:187], s[42:43], 0, v[168:169]
	s_addc_u32 s47, s43, 0
	s_add_i32 s70, s64, s50
	global_load_lds_dwordx4 v[186:187], off
	v_lshl_add_u64 v[188:189], s[46:47], 0, v[164:165]
	s_mov_b32 m0, s70
	v_lshl_add_u64 v[240:241], s[44:45], 0, v[166:167]
	global_load_lds_dwordx4 v[188:189], off
	v_lshl_add_u64 v[188:189], s[46:47], 0, v[168:169]
	s_add_i32 m0, s70, 0x2000
	s_nop 0
	global_load_lds_dwordx4 v[188:189], off
	s_waitcnt vmcnt(6)
	s_waitcnt lgkmcnt(0)
	s_barrier
	s_setprio 1
	s_waitcnt lgkmcnt(0)
	v_mfma_scale_f32_32x32x64_f8f6f4 v[50:65], v[130:137], v[208:215], v[50:65], v193, v193 op_sel_hi:[0,0,0]
	v_mfma_scale_f32_32x32x64_f8f6f4 v[18:33], v[130:137], v[224:231], v[18:33], v193, v193 op_sel_hi:[0,0,0]
	v_mfma_scale_f32_32x32x64_f8f6f4 v[50:65], v[138:145], v[216:223], v[50:65], v193, v193 op_sel_hi:[0,0,0]
	v_lshl_add_u64 v[188:189], s[44:45], 0, v[162:163]
	s_mov_b32 m0, s51
	s_nop 0
	global_load_lds_dwordx4 v[188:189], off
	v_mfma_scale_f32_32x32x64_f8f6f4 v[18:33], v[138:145], v[232:239], v[18:33], v193, v193 op_sel_hi:[0,0,0]
	s_setprio 0
	s_setprio 1
	v_mfma_scale_f32_32x32x64_f8f6f4 v[34:49], v[146:153], v[208:215], v[34:49], v193, v193 op_sel_hi:[0,0,0]
	v_mfma_scale_f32_32x32x64_f8f6f4 v[2:17], v[146:153], v[224:231], v[2:17], v193, v193 op_sel_hi:[0,0,0]
	s_mov_b32 m0, s52
	s_nop 0
	global_load_lds_dwordx4 v[240:241], off
	v_mfma_scale_f32_32x32x64_f8f6f4 v[34:49], v[154:161], v[216:223], v[34:49], v193, v193 op_sel_hi:[0,0,0]
	v_mfma_scale_f32_32x32x64_f8f6f4 v[2:17], v[154:161], v[232:239], v[2:17], v193, v193 op_sel_hi:[0,0,0]
	s_setprio 0
	s_barrier
	s_add_i32 s46, 0, 0x18000
	s_add_i32 s47, 0, 0x1c000
	v_add_u32_e32 v130, s46, v1
	v_add_u32_e32 v134, s46, v177
	v_add_u32_e32 v146, s47, v1
	v_add_u32_e32 v150, s47, v177
	ds_read_b128 v[130:133], v130
	ds_read_b128 v[134:137], v134
	ds_read_b128 v[138:141], v194
	ds_read_b128 v[142:145], v195
	ds_read_b128 v[146:149], v146
	ds_read_b128 v[150:153], v150
	ds_read_b128 v[154:157], v196
	ds_read_b128 v[158:161], v197
	s_add_u32 s44, s44, 0x40000
	s_addc_u32 s45, s45, 0
	s_mov_b32 m0, s53
	v_lshl_add_u64 v[242:243], s[44:45], 0, v[162:163]
	ds_read_b128 v[208:211], v191 offset:32768
	ds_read_b128 v[216:219], v191 offset:33792
	ds_read_b128 v[212:215], v192 offset:32768
	ds_read_b128 v[220:223], v192 offset:33792
	ds_read_b128 v[224:227], v191 offset:36864
	ds_read_b128 v[232:235], v191 offset:37888
	ds_read_b128 v[228:231], v192 offset:36864
	ds_read_b128 v[236:239], v192 offset:37888
	global_load_lds_dwordx4 v[242:243], off
	v_lshl_add_u64 v[242:243], s[44:45], 0, v[166:167]
	s_mov_b32 m0, s54
	s_nop 0
	global_load_lds_dwordx4 v[242:243], off
	s_waitcnt vmcnt(8)
	s_waitcnt lgkmcnt(0)
	s_barrier
	s_setprio 1
	s_waitcnt lgkmcnt(0)
	v_mfma_scale_f32_32x32x64_f8f6f4 v[114:129], v[130:137], v[208:215], v[114:129], v193, v193 op_sel_hi:[0,0,0]
	v_mfma_scale_f32_32x32x64_f8f6f4 v[82:97], v[130:137], v[224:231], v[82:97], v193, v193 op_sel_hi:[0,0,0]
	v_mfma_scale_f32_32x32x64_f8f6f4 v[114:129], v[138:145], v[216:223], v[114:129], v193, v193 op_sel_hi:[0,0,0]
	v_mfma_scale_f32_32x32x64_f8f6f4 v[82:97], v[138:145], v[232:239], v[82:97], v193, v193 op_sel_hi:[0,0,0]
	s_setprio 0
	s_setprio 1
	v_mfma_scale_f32_32x32x64_f8f6f4 v[98:113], v[146:153], v[208:215], v[98:113], v193, v193 op_sel_hi:[0,0,0]
	v_mfma_scale_f32_32x32x64_f8f6f4 v[66:81], v[146:153], v[224:231], v[66:81], v193, v193 op_sel_hi:[0,0,0]
	v_mfma_scale_f32_32x32x64_f8f6f4 v[98:113], v[154:161], v[216:223], v[98:113], v193, v193 op_sel_hi:[0,0,0]
	v_mfma_scale_f32_32x32x64_f8f6f4 v[66:81], v[154:161], v[232:239], v[66:81], v193, v193 op_sel_hi:[0,0,0]
	s_setprio 0
	s_barrier
	s_add_i32 s44, s46, s50
	v_lshl_add_u64 v[184:185], v[184:185], 0, s[20:21]
	s_mov_b32 m0, s44
	ds_read_b128 v[208:211], v191 offset:49152
	ds_read_b128 v[216:219], v191 offset:50176
	ds_read_b128 v[212:215], v192 offset:49152
	ds_read_b128 v[220:223], v192 offset:50176
	ds_read_b128 v[224:227], v191 offset:53248
	ds_read_b128 v[232:235], v191 offset:54272
	ds_read_b128 v[228:231], v192 offset:53248
	ds_read_b128 v[236:239], v192 offset:54272
	global_load_lds_dwordx4 v[184:185], off
	s_add_i32 m0, s44, 0x2000
	s_add_u32 s42, s42, 0x40080
	v_lshl_add_u64 v[184:185], v[186:187], 0, s[20:21]
	s_addc_u32 s43, s43, 0
	s_add_i32 s44, s47, s50
	global_load_lds_dwordx4 v[184:185], off
	v_lshl_add_u64 v[184:185], s[42:43], 0, v[164:165]
	s_mov_b32 m0, s44
	s_nop 0
	global_load_lds_dwordx4 v[184:185], off
	v_lshl_add_u64 v[184:185], s[42:43], 0, v[168:169]
	s_add_i32 m0, s44, 0x2000
	s_nop 0
	global_load_lds_dwordx4 v[184:185], off
	s_waitcnt vmcnt(6)
	s_waitcnt lgkmcnt(0)
	s_barrier
	s_setprio 1
	s_waitcnt lgkmcnt(0)
	v_mfma_scale_f32_32x32x64_f8f6f4 v[50:65], v[130:137], v[208:215], v[50:65], v193, v193 op_sel_hi:[0,0,0]
	v_mfma_scale_f32_32x32x64_f8f6f4 v[18:33], v[130:137], v[224:231], v[18:33], v193, v193 op_sel_hi:[0,0,0]
	v_mfma_scale_f32_32x32x64_f8f6f4 v[50:65], v[138:145], v[216:223], v[50:65], v193, v193 op_sel_hi:[0,0,0]
	v_lshl_add_u64 v[184:185], v[188:189], 0, s[20:21]
	s_mov_b32 m0, s57
	s_nop 0
	global_load_lds_dwordx4 v[184:185], off
	v_mfma_scale_f32_32x32x64_f8f6f4 v[18:33], v[138:145], v[232:239], v[18:33], v193, v193 op_sel_hi:[0,0,0]
	s_setprio 0
	s_setprio 1
	v_mfma_scale_f32_32x32x64_f8f6f4 v[34:49], v[146:153], v[208:215], v[34:49], v193, v193 op_sel_hi:[0,0,0]
	v_mfma_scale_f32_32x32x64_f8f6f4 v[2:17], v[146:153], v[224:231], v[2:17], v193, v193 op_sel_hi:[0,0,0]
	v_lshl_add_u64 v[184:185], v[240:241], 0, s[20:21]
	s_mov_b32 m0, s58
	s_nop 0
	global_load_lds_dwordx4 v[184:185], off
	v_mfma_scale_f32_32x32x64_f8f6f4 v[34:49], v[154:161], v[216:223], v[34:49], v193, v193 op_sel_hi:[0,0,0]
	v_mfma_scale_f32_32x32x64_f8f6f4 v[2:17], v[154:161], v[232:239], v[2:17], v193, v193 op_sel_hi:[0,0,0]
	s_setprio 0
	s_barrier
	s_add_i32 s35, s35, 2
	s_add_u32 s40, s40, 0x100
	s_addc_u32 s41, s41, 0
	s_add_u32 s7, s7, 0x100
	s_addc_u32 s31, s31, 0
	s_cmp_gt_u32 s35, 13
	s_cbranch_scc0 .LBB0_1147
	s_and_b64 vcc, exec, s[22:23]
	s_cbranch_vccz .LBB0_1150
	s_barrier

.LBB0_1536:
	s_waitcnt vmcnt(8)
	s_add_u32 s34, s28, 0x80
	s_waitcnt lgkmcnt(0)
	s_addc_u32 s35, s29, 0
	s_and_b64 s[30:31], s[30:31], exec
	v_mov_b32_e32 v205, v199
	s_cselect_b32 s35, s9, s35
	s_cselect_b32 s34, s8, s34
	s_cselect_b32 s31, s21, s25
	s_cselect_b32 s30, s20, s23
	s_barrier
	s_setprio 1
	s_waitcnt lgkmcnt(0)
	v_mfma_scale_f32_32x32x64_f8f6f4 v[114:129], v[154:161], v[178:185], v[114:129], v224, v224 op_sel_hi:[0,0,0]
	v_mfma_scale_f32_32x32x64_f8f6f4 v[82:97], v[154:161], v[186:193], v[82:97], v224, v224 op_sel_hi:[0,0,0]
	v_mfma_scale_f32_32x32x64_f8f6f4 v[114:129], v[146:153], v[162:169], v[114:129], v224, v224 op_sel_hi:[0,0,0]
	v_mfma_scale_f32_32x32x64_f8f6f4 v[82:97], v[146:153], v[170:177], v[82:97], v224, v224 op_sel_hi:[0,0,0]
	s_setprio 0
	s_setprio 1
	v_mfma_scale_f32_32x32x64_f8f6f4 v[98:113], v[138:145], v[178:185], v[98:113], v224, v224 op_sel_hi:[0,0,0]
	v_mfma_scale_f32_32x32x64_f8f6f4 v[66:81], v[138:145], v[186:193], v[66:81], v224, v224 op_sel_hi:[0,0,0]
	v_mfma_scale_f32_32x32x64_f8f6f4 v[98:113], v[130:137], v[162:169], v[98:113], v224, v224 op_sel_hi:[0,0,0]
	v_mfma_scale_f32_32x32x64_f8f6f4 v[66:81], v[130:137], v[170:177], v[66:81], v224, v224 op_sel_hi:[0,0,0]
	s_setprio 0
	s_barrier
	s_mov_b32 m0, s40
	v_lshl_add_u64 v[232:233], s[30:31], 0, v[194:195]
	s_add_u32 s64, s30, 0x40000
	ds_read_b128 v[162:165], v221 offset:16384
	ds_read_b128 v[170:173], v221 offset:17408
	ds_read_b128 v[166:169], v223 offset:16384
	ds_read_b128 v[174:177], v223 offset:17408
	ds_read_b128 v[178:181], v221 offset:20480
	ds_read_b128 v[186:189], v221 offset:21504
	ds_read_b128 v[182:185], v223 offset:20480
	ds_read_b128 v[190:193], v223 offset:21504
	global_load_lds_dwordx4 v[232:233], off
	v_lshl_add_u64 v[234:235], s[30:31], 0, v[196:197]
	s_mov_b32 m0, s41
	s_addc_u32 s65, s31, 0
	global_load_lds_dwordx4 v[234:235], off
	v_lshl_add_u64 v[236:237], s[64:65], 0, v[194:195]
	s_mov_b32 m0, s42
	v_mov_b32_e32 v203, v199
	global_load_lds_dwordx4 v[236:237], off
	v_lshl_add_u64 v[236:237], s[64:65], 0, v[196:197]
	s_mov_b32 m0, s43
	v_lshl_add_u64 v[238:239], s[34:35], 0, v[202:203]
	global_load_lds_dwordx4 v[236:237], off
	s_waitcnt vmcnt(6)
	s_waitcnt lgkmcnt(0)
	s_barrier
	s_setprio 1
	s_waitcnt lgkmcnt(0)
	v_mfma_scale_f32_32x32x64_f8f6f4 v[50:65], v[154:161], v[162:169], v[50:65], v224, v224 op_sel_hi:[0,0,0]
	v_mfma_scale_f32_32x32x64_f8f6f4 v[18:33], v[154:161], v[178:185], v[18:33], v224, v224 op_sel_hi:[0,0,0]
	v_mfma_scale_f32_32x32x64_f8f6f4 v[50:65], v[146:153], v[170:177], v[50:65], v224, v224 op_sel_hi:[0,0,0]
	s_mov_b32 m0, s39
	v_lshl_add_u64 v[236:237], s[34:35], 0, v[198:199]
	global_load_lds_dwordx4 v198, s[34:35]
	v_mfma_scale_f32_32x32x64_f8f6f4 v[18:33], v[146:153], v[186:193], v[18:33], v224, v224 op_sel_hi:[0,0,0]
	s_setprio 0
	s_setprio 1
	v_mfma_scale_f32_32x32x64_f8f6f4 v[34:49], v[138:145], v[162:169], v[34:49], v224, v224 op_sel_hi:[0,0,0]
	v_mfma_scale_f32_32x32x64_f8f6f4 v[2:17], v[138:145], v[178:185], v[2:17], v224, v224 op_sel_hi:[0,0,0]
	s_mov_b32 m0, s44
	s_nop 0
	global_load_lds_dwordx4 v202, s[34:35]
	v_mfma_scale_f32_32x32x64_f8f6f4 v[34:49], v[130:137], v[170:177], v[34:49], v224, v224 op_sel_hi:[0,0,0]
	v_mfma_scale_f32_32x32x64_f8f6f4 v[2:17], v[130:137], v[186:193], v[2:17], v224, v224 op_sel_hi:[0,0,0]
	s_setprio 0
	s_barrier
	s_add_i32 s63, 0, 0x18000
	s_add_i32 s64, 0, 0x1c000
	v_add_u32_e32 v130, s63, v210
	v_add_u32_e32 v134, s63, v211
	v_add_u32_e32 v138, s55, v210
	v_add_u32_e32 v142, s55, v211
	v_add_u32_e32 v146, s64, v210
	v_add_u32_e32 v150, s64, v211
	v_add_u32_e32 v154, s56, v210
	v_add_u32_e32 v158, s56, v211
	ds_read_b128 v[130:133], v130
	ds_read_b128 v[134:137], v134
	ds_read_b128 v[138:141], v138
	ds_read_b128 v[142:145], v142
	ds_read_b128 v[146:149], v146
	ds_read_b128 v[150:153], v150
	ds_read_b128 v[154:157], v154
	ds_read_b128 v[158:161], v158
	s_mov_b32 m0, s45
	v_lshl_add_u64 v[240:241], s[34:35], 0, v[200:201]
	ds_read_b128 v[162:165], v221 offset:32768
	ds_read_b128 v[170:173], v221 offset:33792
	ds_read_b128 v[166:169], v223 offset:32768
	ds_read_b128 v[174:177], v223 offset:33792
	ds_read_b128 v[178:181], v221 offset:36864
	ds_read_b128 v[186:189], v221 offset:37888
	ds_read_b128 v[182:185], v223 offset:36864
	ds_read_b128 v[190:193], v223 offset:37888
	global_load_lds_dwordx4 v[240:241], off
	v_lshl_add_u64 v[240:241], s[34:35], 0, v[204:205]
	s_mov_b32 m0, s46
	s_nop 0
	global_load_lds_dwordx4 v[240:241], off
	s_waitcnt vmcnt(8)
	s_waitcnt lgkmcnt(0)
	s_barrier
	s_setprio 1
	s_waitcnt lgkmcnt(0)
	v_mfma_scale_f32_32x32x64_f8f6f4 v[114:129], v[130:137], v[162:169], v[114:129], v224, v224 op_sel_hi:[0,0,0]
	v_mfma_scale_f32_32x32x64_f8f6f4 v[82:97], v[130:137], v[178:185], v[82:97], v224, v224 op_sel_hi:[0,0,0]
	v_mfma_scale_f32_32x32x64_f8f6f4 v[114:129], v[138:145], v[170:177], v[114:129], v224, v224 op_sel_hi:[0,0,0]
	v_mfma_scale_f32_32x32x64_f8f6f4 v[82:97], v[138:145], v[186:193], v[82:97], v224, v224 op_sel_hi:[0,0,0]
	s_setprio 0
	s_setprio 1
	v_mfma_scale_f32_32x32x64_f8f6f4 v[98:113], v[146:153], v[162:169], v[98:113], v224, v224 op_sel_hi:[0,0,0]
	v_mfma_scale_f32_32x32x64_f8f6f4 v[66:81], v[146:153], v[178:185], v[66:81], v224, v224 op_sel_hi:[0,0,0]
	v_mfma_scale_f32_32x32x64_f8f6f4 v[98:113], v[154:161], v[170:177], v[98:113], v224, v224 op_sel_hi:[0,0,0]
	v_mfma_scale_f32_32x32x64_f8f6f4 v[66:81], v[154:161], v[186:193], v[66:81], v224, v224 op_sel_hi:[0,0,0]
	s_setprio 0
	s_barrier
	s_add_i32 s34, s63, s38
	v_lshl_add_u64 v[232:233], v[232:233], 0, s[12:13]
	s_mov_b32 m0, s34
	ds_read_b128 v[162:165], v221 offset:49152
	ds_read_b128 v[170:173], v221 offset:50176
	ds_read_b128 v[166:169], v223 offset:49152
	ds_read_b128 v[174:177], v223 offset:50176
	ds_read_b128 v[178:181], v221 offset:53248
	ds_read_b128 v[186:189], v221 offset:54272
	ds_read_b128 v[182:185], v223 offset:53248
	ds_read_b128 v[190:193], v223 offset:54272
	global_load_lds_dwordx4 v[232:233], off
	s_add_i32 m0, s34, 0x2000
	s_add_u32 s30, s30, 0x40080
	v_lshl_add_u64 v[232:233], v[234:235], 0, s[12:13]
	s_addc_u32 s31, s31, 0
	s_add_i32 s34, s64, s38
	global_load_lds_dwordx4 v[232:233], off
	v_lshl_add_u64 v[232:233], s[30:31], 0, v[194:195]
	s_mov_b32 m0, s34
	s_nop 0
	global_load_lds_dwordx4 v[232:233], off
	v_lshl_add_u64 v[232:233], s[30:31], 0, v[196:197]
	s_add_i32 m0, s34, 0x2000
	s_nop 0
	global_load_lds_dwordx4 v[232:233], off
	s_waitcnt vmcnt(6)
	s_waitcnt lgkmcnt(0)
	s_barrier
	s_setprio 1
	s_waitcnt lgkmcnt(0)
	v_mfma_scale_f32_32x32x64_f8f6f4 v[50:65], v[130:137], v[162:169], v[50:65], v224, v224 op_sel_hi:[0,0,0]
	v_mfma_scale_f32_32x32x64_f8f6f4 v[18:33], v[130:137], v[178:185], v[18:33], v224, v224 op_sel_hi:[0,0,0]
	v_mfma_scale_f32_32x32x64_f8f6f4 v[50:65], v[138:145], v[170:177], v[50:65], v224, v224 op_sel_hi:[0,0,0]
	v_lshl_add_u64 v[232:233], v[236:237], 0, s[12:13]
	s_mov_b32 m0, s50
	s_nop 0
	global_load_lds_dwordx4 v[232:233], off
	v_mfma_scale_f32_32x32x64_f8f6f4 v[18:33], v[138:145], v[186:193], v[18:33], v224, v224 op_sel_hi:[0,0,0]
	s_setprio 0
	s_setprio 1
	v_mfma_scale_f32_32x32x64_f8f6f4 v[34:49], v[146:153], v[162:169], v[34:49], v224, v224 op_sel_hi:[0,0,0]
	v_mfma_scale_f32_32x32x64_f8f6f4 v[2:17], v[146:153], v[178:185], v[2:17], v224, v224 op_sel_hi:[0,0,0]
	v_lshl_add_u64 v[232:233], v[238:239], 0, s[12:13]
	s_mov_b32 m0, s51
	s_nop 0
	global_load_lds_dwordx4 v[232:233], off
	v_mfma_scale_f32_32x32x64_f8f6f4 v[34:49], v[154:161], v[170:177], v[34:49], v224, v224 op_sel_hi:[0,0,0]
	v_mfma_scale_f32_32x32x64_f8f6f4 v[2:17], v[154:161], v[186:193], v[2:17], v224, v224 op_sel_hi:[0,0,0]
	s_setprio 0
	s_barrier
	s_add_i32 s62, s62, 2
	s_add_u32 s28, s28, 0x100
	s_addc_u32 s29, s29, 0
	s_add_u32 s23, s23, 0x100
	s_addc_u32 s25, s25, 0
	s_cmp_gt_u32 s62, 13
	s_cbranch_scc1 .LBB0_1539

.LBB0_1625:
	ds_read_b128 v[168:171], v150
	ds_read_b128 v[172:175], v151
	ds_read_b128 v[176:179], v152
	ds_read_b128 v[180:183], v153
	ds_read_b128 v[184:187], v154
	ds_read_b128 v[188:191], v155
	ds_read_b128 v[192:195], v156
	ds_read_b128 v[196:199], v157
	s_add_u32 s28, s26, 0xfffe0080
	s_addc_u32 s29, s27, -1
	s_cmp_eq_u32 s56, 4
	s_cselect_b32 s31, s19, s29
	s_cselect_b32 s30, s18, s28
	s_cselect_b32 s29, s21, s25
	s_cselect_b32 s28, s20, s23
	v_lshl_add_u64 v[144:145], s[26:27], 0, v[140:141]
	s_add_i32 m0, s35, 0xc000
	ds_read_b128 v[200:203], v158
	ds_read_b128 v[208:211], v158 offset:1024
	ds_read_b128 v[204:207], v159
	ds_read_b128 v[212:215], v159 offset:1024
	ds_read_b128 v[216:219], v158 offset:4096
	ds_read_b128 v[224:227], v158 offset:5120
	ds_read_b128 v[220:223], v159 offset:4096
	ds_read_b128 v[228:231], v159 offset:5120
	global_load_lds_dwordx4 v[144:145], off
	v_lshl_add_u64 v[144:145], s[26:27], 0, v[142:143]
	s_add_i32 m0, s35, 0xe000
	s_nop 0
	global_load_lds_dwordx4 v[144:145], off
	s_waitcnt vmcnt(8)
	s_waitcnt lgkmcnt(0)
	s_barrier
	s_setprio 1
	s_waitcnt lgkmcnt(0)
	v_mfma_scale_f32_32x32x64_f8f6f4 v[114:129], v[168:175], v[200:207], v[114:129], v160, v160 op_sel_hi:[0,0,0]
	v_mfma_scale_f32_32x32x64_f8f6f4 v[82:97], v[168:175], v[216:223], v[82:97], v160, v160 op_sel_hi:[0,0,0]
	v_mfma_scale_f32_32x32x64_f8f6f4 v[114:129], v[176:183], v[208:215], v[114:129], v160, v160 op_sel_hi:[0,0,0]
	v_mfma_scale_f32_32x32x64_f8f6f4 v[82:97], v[176:183], v[224:231], v[82:97], v160, v160 op_sel_hi:[0,0,0]
	s_setprio 0
	s_setprio 1
	v_mfma_scale_f32_32x32x64_f8f6f4 v[98:113], v[184:191], v[200:207], v[98:113], v160, v160 op_sel_hi:[0,0,0]
	v_mfma_scale_f32_32x32x64_f8f6f4 v[66:81], v[184:191], v[216:223], v[66:81], v160, v160 op_sel_hi:[0,0,0]
	v_mfma_scale_f32_32x32x64_f8f6f4 v[98:113], v[192:199], v[208:215], v[98:113], v160, v160 op_sel_hi:[0,0,0]
	v_mfma_scale_f32_32x32x64_f8f6f4 v[66:81], v[192:199], v[224:231], v[66:81], v160, v160 op_sel_hi:[0,0,0]
	s_setprio 0
	s_barrier
	s_add_i32 s57, s49, s34
	v_lshl_add_u64 v[144:145], s[28:29], 0, v[132:133]
	s_mov_b32 m0, s57
	ds_read_b128 v[200:203], v158 offset:16384
	ds_read_b128 v[208:211], v158 offset:17408
	ds_read_b128 v[204:207], v159 offset:16384
	ds_read_b128 v[212:215], v159 offset:17408
	ds_read_b128 v[216:219], v158 offset:20480
	ds_read_b128 v[224:227], v158 offset:21504
	ds_read_b128 v[220:223], v159 offset:20480
	ds_read_b128 v[228:231], v159 offset:21504
	global_load_lds_dwordx4 v[144:145], off
	s_add_i32 m0, s57, 0x2000
	s_add_u32 s58, s28, 0x20000
	v_lshl_add_u64 v[146:147], s[28:29], 0, v[136:137]
	s_addc_u32 s59, s29, 0
	s_add_i32 s57, s50, s34
	global_load_lds_dwordx4 v[146:147], off
	v_lshl_add_u64 v[232:233], s[58:59], 0, v[132:133]
	s_mov_b32 m0, s57
	v_lshl_add_u64 v[234:235], s[30:31], 0, v[134:135]
	global_load_lds_dwordx4 v[232:233], off
	v_lshl_add_u64 v[232:233], s[58:59], 0, v[136:137]
	s_add_i32 m0, s57, 0x2000
	s_nop 0
	global_load_lds_dwordx4 v[232:233], off
	s_waitcnt vmcnt(6)
	s_waitcnt lgkmcnt(0)
	s_barrier
	s_setprio 1
	s_waitcnt lgkmcnt(0)
	v_mfma_scale_f32_32x32x64_f8f6f4 v[50:65], v[168:175], v[200:207], v[50:65], v160, v160 op_sel_hi:[0,0,0]
	v_mfma_scale_f32_32x32x64_f8f6f4 v[18:33], v[168:175], v[216:223], v[18:33], v160, v160 op_sel_hi:[0,0,0]
	v_mfma_scale_f32_32x32x64_f8f6f4 v[50:65], v[176:183], v[208:215], v[50:65], v160, v160 op_sel_hi:[0,0,0]
	v_lshl_add_u64 v[232:233], s[30:31], 0, v[130:131]
	s_mov_b32 m0, s35
	s_nop 0
	global_load_lds_dwordx4 v[232:233], off
	v_mfma_scale_f32_32x32x64_f8f6f4 v[18:33], v[176:183], v[224:231], v[18:33], v160, v160 op_sel_hi:[0,0,0]
	s_setprio 0
	s_setprio 1
	v_mfma_scale_f32_32x32x64_f8f6f4 v[34:49], v[184:191], v[200:207], v[34:49], v160, v160 op_sel_hi:[0,0,0]
	v_mfma_scale_f32_32x32x64_f8f6f4 v[2:17], v[184:191], v[216:223], v[2:17], v160, v160 op_sel_hi:[0,0,0]
	s_mov_b32 m0, s36
	s_nop 0
	global_load_lds_dwordx4 v[234:235], off
	v_mfma_scale_f32_32x32x64_f8f6f4 v[34:49], v[192:199], v[208:215], v[34:49], v160, v160 op_sel_hi:[0,0,0]
	v_mfma_scale_f32_32x32x64_f8f6f4 v[2:17], v[192:199], v[224:231], v[2:17], v160, v160 op_sel_hi:[0,0,0]
	s_setprio 0
	s_barrier
	s_add_i32 s57, 0, 0x18000
	v_add_u32_e32 v167, s57, v1
	v_add_u32_e32 v172, s57, v148
	s_add_i32 s58, 0, 0x1c000
	ds_read_b128 v[168:171], v167
	ds_read_b128 v[172:175], v172
	ds_read_b128 v[176:179], v161
	ds_read_b128 v[180:183], v162
	v_add_u32_e32 v167, s58, v1
	v_add_u32_e32 v188, s58, v148
	ds_read_b128 v[184:187], v167
	ds_read_b128 v[188:191], v188
	ds_read_b128 v[192:195], v163
	ds_read_b128 v[196:199], v164
	s_add_u32 s30, s30, 0x20000
	s_addc_u32 s31, s31, 0
	s_mov_b32 m0, s37
	v_lshl_add_u64 v[236:237], s[30:31], 0, v[130:131]
	ds_read_b128 v[200:203], v158 offset:32768
	ds_read_b128 v[208:211], v158 offset:33792
	ds_read_b128 v[204:207], v159 offset:32768
	ds_read_b128 v[212:215], v159 offset:33792
	ds_read_b128 v[216:219], v158 offset:36864
	ds_read_b128 v[224:227], v158 offset:37888
	ds_read_b128 v[220:223], v159 offset:36864
	ds_read_b128 v[228:231], v159 offset:37888
	global_load_lds_dwordx4 v[236:237], off
	v_lshl_add_u64 v[236:237], s[30:31], 0, v[134:135]
	s_mov_b32 m0, s38
	s_nop 0
	global_load_lds_dwordx4 v[236:237], off
	s_waitcnt vmcnt(8)
	s_waitcnt lgkmcnt(0)
	s_barrier
	s_setprio 1
	s_waitcnt lgkmcnt(0)
	v_mfma_scale_f32_32x32x64_f8f6f4 v[114:129], v[168:175], v[200:207], v[114:129], v160, v160 op_sel_hi:[0,0,0]
	v_mfma_scale_f32_32x32x64_f8f6f4 v[82:97], v[168:175], v[216:223], v[82:97], v160, v160 op_sel_hi:[0,0,0]
	v_mfma_scale_f32_32x32x64_f8f6f4 v[114:129], v[176:183], v[208:215], v[114:129], v160, v160 op_sel_hi:[0,0,0]
	v_mfma_scale_f32_32x32x64_f8f6f4 v[82:97], v[176:183], v[224:231], v[82:97], v160, v160 op_sel_hi:[0,0,0]
	s_setprio 0
	s_setprio 1
	v_mfma_scale_f32_32x32x64_f8f6f4 v[98:113], v[184:191], v[200:207], v[98:113], v160, v160 op_sel_hi:[0,0,0]
	v_mfma_scale_f32_32x32x64_f8f6f4 v[66:81], v[184:191], v[216:223], v[66:81], v160, v160 op_sel_hi:[0,0,0]
	v_mfma_scale_f32_32x32x64_f8f6f4 v[98:113], v[192:199], v[208:215], v[98:113], v160, v160 op_sel_hi:[0,0,0]
	v_mfma_scale_f32_32x32x64_f8f6f4 v[66:81], v[192:199], v[224:231], v[66:81], v160, v160 op_sel_hi:[0,0,0]
	s_setprio 0
	s_barrier
	s_add_i32 s30, s57, s34
	v_lshl_add_u64 v[144:145], v[144:145], 0, s[10:11]
	s_mov_b32 m0, s30
	ds_read_b128 v[200:203], v158 offset:49152
	ds_read_b128 v[208:211], v158 offset:50176
	ds_read_b128 v[204:207], v159 offset:49152
	ds_read_b128 v[212:215], v159 offset:50176
	ds_read_b128 v[216:219], v158 offset:53248
	ds_read_b128 v[224:227], v158 offset:54272
	ds_read_b128 v[220:223], v159 offset:53248
	ds_read_b128 v[228:231], v159 offset:54272
	global_load_lds_dwordx4 v[144:145], off
	s_add_i32 m0, s30, 0x2000
	s_add_u32 s28, s28, 0x20080
	v_lshl_add_u64 v[144:145], v[146:147], 0, s[10:11]
	s_addc_u32 s29, s29, 0
	s_add_i32 s30, s58, s34
	global_load_lds_dwordx4 v[144:145], off
	v_lshl_add_u64 v[144:145], s[28:29], 0, v[132:133]
	s_mov_b32 m0, s30
	s_nop 0
	global_load_lds_dwordx4 v[144:145], off
	v_lshl_add_u64 v[144:145], s[28:29], 0, v[136:137]
	s_add_i32 m0, s30, 0x2000
	s_nop 0
	global_load_lds_dwordx4 v[144:145], off
	s_waitcnt vmcnt(6)
	s_waitcnt lgkmcnt(0)
	s_barrier
	s_setprio 1
	s_waitcnt lgkmcnt(0)
	v_mfma_scale_f32_32x32x64_f8f6f4 v[50:65], v[168:175], v[200:207], v[50:65], v160, v160 op_sel_hi:[0,0,0]
	v_mfma_scale_f32_32x32x64_f8f6f4 v[18:33], v[168:175], v[216:223], v[18:33], v160, v160 op_sel_hi:[0,0,0]
	v_mfma_scale_f32_32x32x64_f8f6f4 v[50:65], v[176:183], v[208:215], v[50:65], v160, v160 op_sel_hi:[0,0,0]
	v_lshl_add_u64 v[144:145], v[232:233], 0, s[10:11]
	s_mov_b32 m0, s44
	s_nop 0
	global_load_lds_dwordx4 v[144:145], off
	v_mfma_scale_f32_32x32x64_f8f6f4 v[18:33], v[176:183], v[224:231], v[18:33], v160, v160 op_sel_hi:[0,0,0]
	s_setprio 0
	s_setprio 1
	v_mfma_scale_f32_32x32x64_f8f6f4 v[34:49], v[184:191], v[200:207], v[34:49], v160, v160 op_sel_hi:[0,0,0]
	v_mfma_scale_f32_32x32x64_f8f6f4 v[2:17], v[184:191], v[216:223], v[2:17], v160, v160 op_sel_hi:[0,0,0]
	v_lshl_add_u64 v[144:145], v[234:235], 0, s[10:11]
	s_mov_b32 m0, s45
	s_nop 0
	global_load_lds_dwordx4 v[144:145], off
	v_mfma_scale_f32_32x32x64_f8f6f4 v[34:49], v[192:199], v[208:215], v[34:49], v160, v160 op_sel_hi:[0,0,0]
	v_mfma_scale_f32_32x32x64_f8f6f4 v[2:17], v[192:199], v[224:231], v[2:17], v160, v160 op_sel_hi:[0,0,0]
	s_setprio 0
	s_barrier
	s_add_i32 s56, s56, 2
	s_add_u32 s26, s26, 0x100
	s_addc_u32 s27, s27, 0
	s_add_u32 s23, s23, 0x100
	s_addc_u32 s25, s25, 0
	s_cmp_gt_u32 s56, 5
	s_cbranch_scc0 .LBB0_1625
	s_and_b64 vcc, exec, s[12:13]
	s_cbranch_vccz .LBB0_1628
	s_barrier
